# speedup vs baseline: 1.0299x; 1.0299x over previous
_Z11center_mainPKfPKcS0_Pf:
	s_load_dwordx4 s[4:7], s[0:1], 0x0
	s_load_dwordx4 s[8:11], s[0:1], 0x10
	s_and_b32 s3, s2, 7
	s_lshr_b32 s12, s2, 3
	s_mov_b32 s30, s2
	v_lshrrev_b32_e32 v1, 6, v0
	v_and_b32_e32 v2, 63, v0
	v_bfe_u32 v3, v0, 3, 3
	v_and_b32_e32 v4, 7, v0
	v_lshrrev_b32_e32 v5, 7, v0
	v_bfe_u32 v6, v0, 6, 1
	v_lshl_or_b32 v7, v5, 3, v3
	v_lshlrev_b32_e32 v8, 10, v7
	v_lshl_or_b32 v8, v6, 9, v8
	v_lshl_or_b32 v226, v4, 4, v8
	v_lshlrev_b32_e32 v17, 15, v1
	v_lshl_or_b32 v227, v2, 5, v17
	v_lshlrev_b32_e32 v237, 3, v0
	s_lshl_b32 s13, s3, 22
	s_lshl_b32 s14, s12, 15
	s_add_u32 s13, s13, s14
	s_lshl_b32 s15, s3, 18
	s_lshl_b32 s28, s3, 12
	s_waitcnt lgkmcnt(0)
	s_add_u32 s16, s4, s13
	s_addc_u32 s17, s5, 0
	global_load_dwordx4 v[194:197], v226, s[16:17] offset:0 nt
	global_load_dwordx4 v[198:201], v226, s[16:17] offset:128 nt
	global_load_dwordx4 v[202:205], v226, s[16:17] offset:256 nt
	global_load_dwordx4 v[206:209], v226, s[16:17] offset:384 nt
	s_add_u32 s8, s8, s28
	s_addc_u32 s9, s9, 0
	global_load_dwordx2 v[238:239], v237, s[8:9]
	s_add_u32 s24, s6, s15
	s_addc_u32 s25, s7, 0
	s_add_u32 s32, s24, 0x1000
	s_addc_u32 s33, s25, 0
	s_add_u32 s34, s24, 0x2000
	s_addc_u32 s35, s25, 0
	s_add_u32 s36, s24, 0x3000
	s_addc_u32 s37, s25, 0
	s_add_u32 s38, s24, 0x4000
	s_addc_u32 s39, s25, 0
	s_add_u32 s40, s24, 0x5000
	s_addc_u32 s41, s25, 0
	s_add_u32 s42, s24, 0x6000
	s_addc_u32 s43, s25, 0
	s_add_u32 s44, s24, 0x7000
	s_addc_u32 s45, s25, 0
	global_load_dwordx4 v[34:37], v227, s[24:25] offset:0
	global_load_dwordx4 v[38:41], v227, s[24:25] offset:16
	global_load_dwordx4 v[26:29], v227, s[24:25] offset:2048
	global_load_dwordx4 v[30:33], v227, s[24:25] offset:2064
	global_load_dwordx4 v[50:53], v227, s[32:33] offset:0
	global_load_dwordx4 v[54:57], v227, s[32:33] offset:16
	global_load_dwordx4 v[42:45], v227, s[32:33] offset:2048
	global_load_dwordx4 v[46:49], v227, s[32:33] offset:2064
	global_load_dwordx4 v[18:21], v227, s[34:35] offset:0
	global_load_dwordx4 v[22:25], v227, s[34:35] offset:16
	global_load_dwordx4 v[130:133], v227, s[34:35] offset:2048
	global_load_dwordx4 v[134:137], v227, s[34:35] offset:2064
	global_load_dwordx4 v[122:125], v227, s[36:37] offset:0
	global_load_dwordx4 v[126:129], v227, s[36:37] offset:16
	global_load_dwordx4 v[138:141], v227, s[36:37] offset:2048
	global_load_dwordx4 v[142:145], v227, s[36:37] offset:2064
	global_load_dwordx4 v[98:101], v227, s[38:39] offset:0
	global_load_dwordx4 v[102:105], v227, s[38:39] offset:16
	global_load_dwordx4 v[90:93], v227, s[38:39] offset:2048
	global_load_dwordx4 v[94:97], v227, s[38:39] offset:2064
	global_load_dwordx4 v[114:117], v227, s[40:41] offset:0
	global_load_dwordx4 v[118:121], v227, s[40:41] offset:16
	global_load_dwordx4 v[106:109], v227, s[40:41] offset:2048
	global_load_dwordx4 v[110:113], v227, s[40:41] offset:2064
	global_load_dwordx4 v[58:61], v227, s[42:43] offset:0
	global_load_dwordx4 v[62:65], v227, s[42:43] offset:16
	global_load_dwordx4 v[66:69], v227, s[42:43] offset:2048
	global_load_dwordx4 v[70:73], v227, s[42:43] offset:2064
	global_load_dwordx4 v[74:77], v227, s[44:45] offset:0
	global_load_dwordx4 v[78:81], v227, s[44:45] offset:16
	global_load_dwordx4 v[82:85], v227, s[44:45] offset:2048
	global_load_dwordx4 v[86:89], v227, s[44:45] offset:2064
	s_add_u32 s18, s16, 0x100000
	s_addc_u32 s19, s17, 0
	s_add_u32 s20, s16, 0x200000
	s_addc_u32 s21, s17, 0
	s_add_u32 s22, s16, 0x300000
	s_addc_u32 s23, s17, 0
	v_mul_u32_u24_e32 v9, 0x110, v7
	v_lshl_add_u32 v9, v6, 7, v9
	v_lshl_add_u32 v228, v4, 4, v9
	v_lshlrev_b32_e32 v10, 6, v7
	v_lshl_or_b32 v10, v6, 5, v10
	v_lshl_or_b32 v229, v4, 2, v10
	v_and_b32_e32 v11, 31, v0
	v_bfe_u32 v12, v0, 5, 1
	v_mul_u32_u24_e32 v13, 0x110, v11
	v_lshl_add_u32 v230, v12, 5, v13
	v_lshlrev_b32_e32 v14, 9, v1
	v_lshl_or_b32 v231, v12, 4, v14
	v_xor_b32_e32 v15, 32, v2
	v_lshlrev_b32_e32 v232, 2, v15
	v_xor_b32_e32 v15, 16, v2
	v_lshlrev_b32_e32 v247, 2, v15
	v_lshlrev_b32_e32 v16, 7, v1
	v_lshl_or_b32 v233, v11, 2, v16
	v_mov_b32_e32 v234, 0x7f7f7f7f
	s_waitcnt vmcnt(32)
	ds_write_b64 v237, v[238:239] offset:34816
	v_mul_f32_e32 v244, v194, v194
	v_mul_f32_e32 v245, v198, v198
	v_cvt_pk_fp8_f32 v240, v194, v195
	v_cvt_pk_fp8_f32 v241, v198, v199
	v_cvt_pk_fp8_f32 v242, v202, v203
	v_cvt_pk_fp8_f32 v243, v206, v207
	v_fmac_f32_e32 v244, v195, v195
	v_fmac_f32_e32 v245, v199, v199
	v_fmac_f32_e32 v244, v196, v196
	v_fmac_f32_e32 v245, v200, v200
	v_fmac_f32_e32 v244, v197, v197
	v_fmac_f32_e32 v245, v201, v201
	v_fmac_f32_e32 v244, v202, v202
	v_fmac_f32_e32 v245, v206, v206
	v_fmac_f32_e32 v244, v203, v203
	v_fmac_f32_e32 v245, v207, v207
	v_fmac_f32_e32 v244, v204, v204
	v_fmac_f32_e32 v245, v208, v208
	v_fmac_f32_e32 v244, v205, v205
	v_fmac_f32_e32 v245, v209, v209
	v_cvt_pk_fp8_f32 v240, v196, v197 op_sel:[0,0,1]
	v_cvt_pk_fp8_f32 v241, v200, v201 op_sel:[0,0,1]
	v_cvt_pk_fp8_f32 v242, v204, v205 op_sel:[0,0,1]
	v_cvt_pk_fp8_f32 v243, v208, v209 op_sel:[0,0,1]
	v_add_f32_e32 v244, v244, v245
	s_nop 0
	ds_write_b128 v228, v[240:243] offset:0
	ds_write_b32 v229, v244 offset:38912
	s_waitcnt lgkmcnt(0)
	s_barrier
	ds_read_b128 v[162:165], v230 offset:0
	ds_read_b128 v[166:169], v230 offset:16
	ds_read_b128 v[2:5], v231 offset:34816
	ds_read_b128 v[6:9], v231 offset:34848
	ds_read_b128 v[10:13], v231 offset:34880
	ds_read_b128 v[14:17], v231 offset:34912
	ds_read_b128 v[170:173], v230 offset:64
	ds_read_b128 v[174:177], v230 offset:80
	ds_read_b128 v[178:181], v230 offset:128
	ds_read_b128 v[182:185], v230 offset:144
	ds_read_b128 v[186:189], v230 offset:192
	ds_read_b128 v[190:193], v230 offset:208
	s_waitcnt vmcnt(30) lgkmcnt(6)
	v_mfma_scale_f32_32x32x64_f8f6f4 v[2:17], v[34:41], v[162:169], v[2:17], v234, v234 op_sel_hi:[0,0,0]
	s_waitcnt vmcnt(28) lgkmcnt(4)
	v_mfma_scale_f32_32x32x64_f8f6f4 v[2:17], v[26:33], v[170:177], v[2:17], v234, v234 op_sel_hi:[0,0,0]
	ds_read_b128 v[146:149], v231 offset:34944
	ds_read_b128 v[150:153], v231 offset:34976
	ds_read_b128 v[154:157], v231 offset:35008
	ds_read_b128 v[158:161], v231 offset:35040
	s_waitcnt vmcnt(26) lgkmcnt(6)
	v_mfma_scale_f32_32x32x64_f8f6f4 v[2:17], v[50:57], v[178:185], v[2:17], v234, v234 op_sel_hi:[0,0,0]
	s_waitcnt vmcnt(24) lgkmcnt(4)
	v_mfma_scale_f32_32x32x64_f8f6f4 v[2:17], v[42:49], v[186:193], v[2:17], v234, v234 op_sel_hi:[0,0,0]
	global_load_dwordx4 v[210:213], v226, s[18:19] offset:0 nt
	global_load_dwordx4 v[214:217], v226, s[18:19] offset:128 nt
	global_load_dwordx4 v[218:221], v226, s[18:19] offset:256 nt
	global_load_dwordx4 v[222:225], v226, s[18:19] offset:384 nt
	s_waitcnt lgkmcnt(0)
	s_waitcnt vmcnt(26)
	v_mfma_scale_f32_32x32x64_f8f6f4 v[146:161], v[18:25], v[162:169], v[146:161], v234, v234 op_sel_hi:[0,0,0]
	s_waitcnt vmcnt(24)
	v_mfma_scale_f32_32x32x64_f8f6f4 v[146:161], v[130:137], v[170:177], v[146:161], v234, v234 op_sel_hi:[0,0,0]
	v_min3_f32 v2, v2, v3, v4
	v_min3_f32 v5, v5, v6, v7
	v_min3_f32 v8, v8, v9, v10
	v_min3_f32 v11, v11, v12, v13
	v_min3_f32 v14, v14, v15, v16
	v_min3_f32 v2, v2, v5, v8
	v_min3_f32 v11, v11, v14, v17
	v_min_f32_e32 v235, v2, v11
	ds_read_b128 v[2:5], v231 offset:35072
	ds_read_b128 v[6:9], v231 offset:35104
	ds_read_b128 v[10:13], v231 offset:35136
	ds_read_b128 v[14:17], v231 offset:35168
	s_waitcnt vmcnt(22)
	v_mfma_scale_f32_32x32x64_f8f6f4 v[146:161], v[122:129], v[178:185], v[146:161], v234, v234 op_sel_hi:[0,0,0]
	s_waitcnt vmcnt(20)
	v_mfma_scale_f32_32x32x64_f8f6f4 v[146:161], v[138:145], v[186:193], v[146:161], v234, v234 op_sel_hi:[0,0,0]
	s_waitcnt vmcnt(18) lgkmcnt(0)
	v_mfma_scale_f32_32x32x64_f8f6f4 v[2:17], v[98:105], v[162:169], v[2:17], v234, v234 op_sel_hi:[0,0,0]
	s_waitcnt vmcnt(16)
	v_mfma_scale_f32_32x32x64_f8f6f4 v[2:17], v[90:97], v[170:177], v[2:17], v234, v234 op_sel_hi:[0,0,0]
	v_min3_f32 v146, v146, v147, v148
	v_min3_f32 v149, v149, v150, v151
	v_min3_f32 v152, v152, v153, v154
	v_min3_f32 v155, v155, v156, v157
	v_min3_f32 v158, v158, v159, v160
	v_min3_f32 v146, v146, v149, v152
	v_min3_f32 v155, v155, v158, v161
	v_min3_f32 v235, v235, v146, v155
	ds_read_b128 v[146:149], v231 offset:35200
	ds_read_b128 v[150:153], v231 offset:35232
	ds_read_b128 v[154:157], v231 offset:35264
	ds_read_b128 v[158:161], v231 offset:35296
	s_waitcnt vmcnt(14)
	v_mfma_scale_f32_32x32x64_f8f6f4 v[2:17], v[114:121], v[178:185], v[2:17], v234, v234 op_sel_hi:[0,0,0]
	s_waitcnt vmcnt(12)
	v_mfma_scale_f32_32x32x64_f8f6f4 v[2:17], v[106:113], v[186:193], v[2:17], v234, v234 op_sel_hi:[0,0,0]
	s_waitcnt vmcnt(10) lgkmcnt(0)
	v_mfma_scale_f32_32x32x64_f8f6f4 v[146:161], v[58:65], v[162:169], v[146:161], v234, v234 op_sel_hi:[0,0,0]
	s_waitcnt vmcnt(8)
	v_mfma_scale_f32_32x32x64_f8f6f4 v[146:161], v[66:73], v[170:177], v[146:161], v234, v234 op_sel_hi:[0,0,0]
	v_min3_f32 v2, v2, v3, v4
	v_min3_f32 v5, v5, v6, v7
	v_min3_f32 v8, v8, v9, v10
	v_min3_f32 v11, v11, v12, v13
	v_min3_f32 v14, v14, v15, v16
	v_min3_f32 v2, v2, v5, v8
	v_min3_f32 v11, v11, v14, v17
	v_min3_f32 v235, v235, v2, v11
	ds_read_b128 v[2:5], v231 offset:34816
	ds_read_b128 v[6:9], v231 offset:34848
	ds_read_b128 v[10:13], v231 offset:34880
	ds_read_b128 v[14:17], v231 offset:34912
	s_waitcnt vmcnt(6)
	v_mfma_scale_f32_32x32x64_f8f6f4 v[146:161], v[74:81], v[178:185], v[146:161], v234, v234 op_sel_hi:[0,0,0]
	s_waitcnt vmcnt(4)
	v_mfma_scale_f32_32x32x64_f8f6f4 v[146:161], v[82:89], v[186:193], v[146:161], v234, v234 op_sel_hi:[0,0,0]
	s_waitcnt vmcnt(0)
	v_mul_f32_e32 v244, v210, v210
	v_mul_f32_e32 v245, v214, v214
	v_cvt_pk_fp8_f32 v240, v210, v211
	v_cvt_pk_fp8_f32 v241, v214, v215
	v_cvt_pk_fp8_f32 v242, v218, v219
	v_cvt_pk_fp8_f32 v243, v222, v223
	v_fmac_f32_e32 v244, v211, v211
	v_fmac_f32_e32 v245, v215, v215
	v_fmac_f32_e32 v244, v212, v212
	v_fmac_f32_e32 v245, v216, v216
	v_fmac_f32_e32 v244, v213, v213
	v_fmac_f32_e32 v245, v217, v217
	v_fmac_f32_e32 v244, v218, v218
	v_fmac_f32_e32 v245, v222, v222
	v_fmac_f32_e32 v244, v219, v219
	v_fmac_f32_e32 v245, v223, v223
	v_fmac_f32_e32 v244, v220, v220
	v_fmac_f32_e32 v245, v224, v224
	v_fmac_f32_e32 v244, v221, v221
	v_fmac_f32_e32 v245, v225, v225
	v_cvt_pk_fp8_f32 v240, v212, v213 op_sel:[0,0,1]
	v_cvt_pk_fp8_f32 v241, v216, v217 op_sel:[0,0,1]
	v_cvt_pk_fp8_f32 v242, v220, v221 op_sel:[0,0,1]
	v_cvt_pk_fp8_f32 v243, v224, v225 op_sel:[0,0,1]
	v_add_f32_e32 v244, v244, v245
	s_nop 0
	ds_write_b128 v228, v[240:243] offset:8704
	ds_write_b32 v229, v244 offset:40960
	global_load_dwordx4 v[194:197], v226, s[20:21] offset:0 nt
	global_load_dwordx4 v[198:201], v226, s[20:21] offset:128 nt
	global_load_dwordx4 v[202:205], v226, s[20:21] offset:256 nt
	global_load_dwordx4 v[206:209], v226, s[20:21] offset:384 nt
	s_waitcnt lgkmcnt(0)
	s_barrier
	ds_read_b128 v[162:165], v230 offset:8704
	ds_read_b128 v[166:169], v230 offset:8720
	ds_read_b128 v[170:173], v230 offset:8768
	ds_read_b128 v[174:177], v230 offset:8784
	ds_read_b128 v[178:181], v230 offset:8832
	ds_read_b128 v[182:185], v230 offset:8848
	ds_read_b128 v[186:189], v230 offset:8896
	ds_read_b128 v[190:193], v230 offset:8912
	s_waitcnt lgkmcnt(6)
	v_mfma_scale_f32_32x32x64_f8f6f4 v[2:17], v[34:41], v[162:169], v[2:17], v234, v234 op_sel_hi:[0,0,0]
	s_waitcnt lgkmcnt(4)
	v_mfma_scale_f32_32x32x64_f8f6f4 v[2:17], v[26:33], v[170:177], v[2:17], v234, v234 op_sel_hi:[0,0,0]
	v_min3_f32 v146, v146, v147, v148
	v_min3_f32 v149, v149, v150, v151
	v_min3_f32 v152, v152, v153, v154
	v_min3_f32 v155, v155, v156, v157
	v_min3_f32 v158, v158, v159, v160
	v_min3_f32 v146, v146, v149, v152
	v_min3_f32 v155, v155, v158, v161
	v_min3_f32 v235, v235, v146, v155
	ds_bpermute_b32 v246, v232, v235
	ds_read_b128 v[146:149], v231 offset:34944
	ds_read_b128 v[150:153], v231 offset:34976
	ds_read_b128 v[154:157], v231 offset:35008
	ds_read_b128 v[158:161], v231 offset:35040
	s_waitcnt lgkmcnt(7)
	v_mfma_scale_f32_32x32x64_f8f6f4 v[2:17], v[50:57], v[178:185], v[2:17], v234, v234 op_sel_hi:[0,0,0]
	s_waitcnt lgkmcnt(5)
	v_mfma_scale_f32_32x32x64_f8f6f4 v[2:17], v[42:49], v[186:193], v[2:17], v234, v234 op_sel_hi:[0,0,0]
	s_waitcnt lgkmcnt(0)
	v_min_f32_e32 v246, v235, v246
	ds_write_b32 v233, v246 offset:47104
	v_mfma_scale_f32_32x32x64_f8f6f4 v[146:161], v[18:25], v[162:169], v[146:161], v234, v234 op_sel_hi:[0,0,0]
	v_mfma_scale_f32_32x32x64_f8f6f4 v[146:161], v[130:137], v[170:177], v[146:161], v234, v234 op_sel_hi:[0,0,0]
	v_min3_f32 v2, v2, v3, v4
	v_min3_f32 v5, v5, v6, v7
	v_min3_f32 v8, v8, v9, v10
	v_min3_f32 v11, v11, v12, v13
	v_min3_f32 v14, v14, v15, v16
	v_min3_f32 v2, v2, v5, v8
	v_min3_f32 v11, v11, v14, v17
	v_min_f32_e32 v236, v2, v11
	ds_read_b128 v[2:5], v231 offset:35072
	ds_read_b128 v[6:9], v231 offset:35104
	ds_read_b128 v[10:13], v231 offset:35136
	ds_read_b128 v[14:17], v231 offset:35168
	v_mfma_scale_f32_32x32x64_f8f6f4 v[146:161], v[122:129], v[178:185], v[146:161], v234, v234 op_sel_hi:[0,0,0]
	v_mfma_scale_f32_32x32x64_f8f6f4 v[146:161], v[138:145], v[186:193], v[146:161], v234, v234 op_sel_hi:[0,0,0]
	s_waitcnt lgkmcnt(0)
	v_mfma_scale_f32_32x32x64_f8f6f4 v[2:17], v[98:105], v[162:169], v[2:17], v234, v234 op_sel_hi:[0,0,0]
	v_mfma_scale_f32_32x32x64_f8f6f4 v[2:17], v[90:97], v[170:177], v[2:17], v234, v234 op_sel_hi:[0,0,0]
	v_min3_f32 v146, v146, v147, v148
	v_min3_f32 v149, v149, v150, v151
	v_min3_f32 v152, v152, v153, v154
	v_min3_f32 v155, v155, v156, v157
	v_min3_f32 v158, v158, v159, v160
	v_min3_f32 v146, v146, v149, v152
	v_min3_f32 v155, v155, v158, v161
	v_min3_f32 v236, v236, v146, v155
	ds_read_b128 v[146:149], v231 offset:35200
	ds_read_b128 v[150:153], v231 offset:35232
	ds_read_b128 v[154:157], v231 offset:35264
	ds_read_b128 v[158:161], v231 offset:35296
	v_mfma_scale_f32_32x32x64_f8f6f4 v[2:17], v[114:121], v[178:185], v[2:17], v234, v234 op_sel_hi:[0,0,0]
	v_mfma_scale_f32_32x32x64_f8f6f4 v[2:17], v[106:113], v[186:193], v[2:17], v234, v234 op_sel_hi:[0,0,0]
	s_waitcnt lgkmcnt(0)
	v_mfma_scale_f32_32x32x64_f8f6f4 v[146:161], v[58:65], v[162:169], v[146:161], v234, v234 op_sel_hi:[0,0,0]
	v_mfma_scale_f32_32x32x64_f8f6f4 v[146:161], v[66:73], v[170:177], v[146:161], v234, v234 op_sel_hi:[0,0,0]
	v_min3_f32 v2, v2, v3, v4
	v_min3_f32 v5, v5, v6, v7
	v_min3_f32 v8, v8, v9, v10
	v_min3_f32 v11, v11, v12, v13
	v_min3_f32 v14, v14, v15, v16
	v_min3_f32 v2, v2, v5, v8
	v_min3_f32 v11, v11, v14, v17
	v_min3_f32 v236, v236, v2, v11
	ds_read_b128 v[2:5], v231 offset:34816
	ds_read_b128 v[6:9], v231 offset:34848
	ds_read_b128 v[10:13], v231 offset:34880
	ds_read_b128 v[14:17], v231 offset:34912
	v_mfma_scale_f32_32x32x64_f8f6f4 v[146:161], v[74:81], v[178:185], v[146:161], v234, v234 op_sel_hi:[0,0,0]
	v_mfma_scale_f32_32x32x64_f8f6f4 v[146:161], v[82:89], v[186:193], v[146:161], v234, v234 op_sel_hi:[0,0,0]
	s_waitcnt vmcnt(0)
	v_mul_f32_e32 v244, v194, v194
	v_mul_f32_e32 v245, v198, v198
	v_cvt_pk_fp8_f32 v240, v194, v195
	v_cvt_pk_fp8_f32 v241, v198, v199
	v_cvt_pk_fp8_f32 v242, v202, v203
	v_cvt_pk_fp8_f32 v243, v206, v207
	v_fmac_f32_e32 v244, v195, v195
	v_fmac_f32_e32 v245, v199, v199
	v_fmac_f32_e32 v244, v196, v196
	v_fmac_f32_e32 v245, v200, v200
	v_fmac_f32_e32 v244, v197, v197
	v_fmac_f32_e32 v245, v201, v201
	v_fmac_f32_e32 v244, v202, v202
	v_fmac_f32_e32 v245, v206, v206
	v_fmac_f32_e32 v244, v203, v203
	v_fmac_f32_e32 v245, v207, v207
	v_fmac_f32_e32 v244, v204, v204
	v_fmac_f32_e32 v245, v208, v208
	v_fmac_f32_e32 v244, v205, v205
	v_fmac_f32_e32 v245, v209, v209
	v_cvt_pk_fp8_f32 v240, v196, v197 op_sel:[0,0,1]
	v_cvt_pk_fp8_f32 v241, v200, v201 op_sel:[0,0,1]
	v_cvt_pk_fp8_f32 v242, v204, v205 op_sel:[0,0,1]
	v_cvt_pk_fp8_f32 v243, v208, v209 op_sel:[0,0,1]
	v_add_f32_e32 v244, v244, v245
	s_nop 0
	ds_write_b128 v228, v[240:243] offset:17408
	ds_write_b32 v229, v244 offset:43008
	global_load_dwordx4 v[210:213], v226, s[22:23] offset:0 nt
	global_load_dwordx4 v[214:217], v226, s[22:23] offset:128 nt
	global_load_dwordx4 v[218:221], v226, s[22:23] offset:256 nt
	global_load_dwordx4 v[222:225], v226, s[22:23] offset:384 nt
	s_waitcnt lgkmcnt(0)
	s_barrier
	ds_read_b128 v[162:165], v230 offset:17408
	ds_read_b128 v[166:169], v230 offset:17424
	ds_read_b128 v[170:173], v230 offset:17472
	ds_read_b128 v[174:177], v230 offset:17488
	ds_read_b128 v[178:181], v230 offset:17536
	ds_read_b128 v[182:185], v230 offset:17552
	ds_read_b128 v[186:189], v230 offset:17600
	ds_read_b128 v[190:193], v230 offset:17616
	s_waitcnt lgkmcnt(6)
	v_mfma_scale_f32_32x32x64_f8f6f4 v[2:17], v[34:41], v[162:169], v[2:17], v234, v234 op_sel_hi:[0,0,0]
	s_waitcnt lgkmcnt(4)
	v_mfma_scale_f32_32x32x64_f8f6f4 v[2:17], v[26:33], v[170:177], v[2:17], v234, v234 op_sel_hi:[0,0,0]
	v_min3_f32 v146, v146, v147, v148
	v_min3_f32 v149, v149, v150, v151
	v_min3_f32 v152, v152, v153, v154
	v_min3_f32 v155, v155, v156, v157
	v_min3_f32 v158, v158, v159, v160
	v_min3_f32 v146, v146, v149, v152
	v_min3_f32 v155, v155, v158, v161
	v_min3_f32 v236, v236, v146, v155
	ds_bpermute_b32 v246, v232, v236
	ds_read_b128 v[146:149], v231 offset:34944
	ds_read_b128 v[150:153], v231 offset:34976
	ds_read_b128 v[154:157], v231 offset:35008
	ds_read_b128 v[158:161], v231 offset:35040
	s_waitcnt lgkmcnt(7)
	v_mfma_scale_f32_32x32x64_f8f6f4 v[2:17], v[50:57], v[178:185], v[2:17], v234, v234 op_sel_hi:[0,0,0]
	s_waitcnt lgkmcnt(5)
	v_mfma_scale_f32_32x32x64_f8f6f4 v[2:17], v[42:49], v[186:193], v[2:17], v234, v234 op_sel_hi:[0,0,0]
	s_waitcnt lgkmcnt(0)
	v_min_f32_e32 v246, v236, v246
	ds_write_b32 v233, v246 offset:48128
	v_mfma_scale_f32_32x32x64_f8f6f4 v[146:161], v[18:25], v[162:169], v[146:161], v234, v234 op_sel_hi:[0,0,0]
	v_mfma_scale_f32_32x32x64_f8f6f4 v[146:161], v[130:137], v[170:177], v[146:161], v234, v234 op_sel_hi:[0,0,0]
	v_min3_f32 v2, v2, v3, v4
	v_min3_f32 v5, v5, v6, v7
	v_min3_f32 v8, v8, v9, v10
	v_min3_f32 v11, v11, v12, v13
	v_min3_f32 v14, v14, v15, v16
	v_min3_f32 v2, v2, v5, v8
	v_min3_f32 v11, v11, v14, v17
	v_min_f32_e32 v235, v2, v11
	ds_read_b128 v[2:5], v231 offset:35072
	ds_read_b128 v[6:9], v231 offset:35104
	ds_read_b128 v[10:13], v231 offset:35136
	ds_read_b128 v[14:17], v231 offset:35168
	v_mfma_scale_f32_32x32x64_f8f6f4 v[146:161], v[122:129], v[178:185], v[146:161], v234, v234 op_sel_hi:[0,0,0]
	v_mfma_scale_f32_32x32x64_f8f6f4 v[146:161], v[138:145], v[186:193], v[146:161], v234, v234 op_sel_hi:[0,0,0]
	s_waitcnt lgkmcnt(0)
	v_mfma_scale_f32_32x32x64_f8f6f4 v[2:17], v[98:105], v[162:169], v[2:17], v234, v234 op_sel_hi:[0,0,0]
	v_mfma_scale_f32_32x32x64_f8f6f4 v[2:17], v[90:97], v[170:177], v[2:17], v234, v234 op_sel_hi:[0,0,0]
	v_min3_f32 v146, v146, v147, v148
	v_min3_f32 v149, v149, v150, v151
	v_min3_f32 v152, v152, v153, v154
	v_min3_f32 v155, v155, v156, v157
	v_min3_f32 v158, v158, v159, v160
	v_min3_f32 v146, v146, v149, v152
	v_min3_f32 v155, v155, v158, v161
	v_min3_f32 v235, v235, v146, v155
	ds_read_b128 v[146:149], v231 offset:35200
	ds_read_b128 v[150:153], v231 offset:35232
	ds_read_b128 v[154:157], v231 offset:35264
	ds_read_b128 v[158:161], v231 offset:35296
	v_mfma_scale_f32_32x32x64_f8f6f4 v[2:17], v[114:121], v[178:185], v[2:17], v234, v234 op_sel_hi:[0,0,0]
	v_mfma_scale_f32_32x32x64_f8f6f4 v[2:17], v[106:113], v[186:193], v[2:17], v234, v234 op_sel_hi:[0,0,0]
	s_waitcnt lgkmcnt(0)
	v_mfma_scale_f32_32x32x64_f8f6f4 v[146:161], v[58:65], v[162:169], v[146:161], v234, v234 op_sel_hi:[0,0,0]
	v_mfma_scale_f32_32x32x64_f8f6f4 v[146:161], v[66:73], v[170:177], v[146:161], v234, v234 op_sel_hi:[0,0,0]
	v_min3_f32 v2, v2, v3, v4
	v_min3_f32 v5, v5, v6, v7
	v_min3_f32 v8, v8, v9, v10
	v_min3_f32 v11, v11, v12, v13
	v_min3_f32 v14, v14, v15, v16
	v_min3_f32 v2, v2, v5, v8
	v_min3_f32 v11, v11, v14, v17
	v_min3_f32 v235, v235, v2, v11
	ds_read_b128 v[2:5], v231 offset:34816
	ds_read_b128 v[6:9], v231 offset:34848
	ds_read_b128 v[10:13], v231 offset:34880
	ds_read_b128 v[14:17], v231 offset:34912
	v_mfma_scale_f32_32x32x64_f8f6f4 v[146:161], v[74:81], v[178:185], v[146:161], v234, v234 op_sel_hi:[0,0,0]
	v_mfma_scale_f32_32x32x64_f8f6f4 v[146:161], v[82:89], v[186:193], v[146:161], v234, v234 op_sel_hi:[0,0,0]
	s_waitcnt vmcnt(0)
	v_mul_f32_e32 v244, v210, v210
	v_mul_f32_e32 v245, v214, v214
	v_cvt_pk_fp8_f32 v240, v210, v211
	v_cvt_pk_fp8_f32 v241, v214, v215
	v_cvt_pk_fp8_f32 v242, v218, v219
	v_cvt_pk_fp8_f32 v243, v222, v223
	v_fmac_f32_e32 v244, v211, v211
	v_fmac_f32_e32 v245, v215, v215
	v_fmac_f32_e32 v244, v212, v212
	v_fmac_f32_e32 v245, v216, v216
	v_fmac_f32_e32 v244, v213, v213
	v_fmac_f32_e32 v245, v217, v217
	v_fmac_f32_e32 v244, v218, v218
	v_fmac_f32_e32 v245, v222, v222
	v_fmac_f32_e32 v244, v219, v219
	v_fmac_f32_e32 v245, v223, v223
	v_fmac_f32_e32 v244, v220, v220
	v_fmac_f32_e32 v245, v224, v224
	v_fmac_f32_e32 v244, v221, v221
	v_fmac_f32_e32 v245, v225, v225
	v_cvt_pk_fp8_f32 v240, v212, v213 op_sel:[0,0,1]
	v_cvt_pk_fp8_f32 v241, v216, v217 op_sel:[0,0,1]
	v_cvt_pk_fp8_f32 v242, v220, v221 op_sel:[0,0,1]
	v_cvt_pk_fp8_f32 v243, v224, v225 op_sel:[0,0,1]
	v_add_f32_e32 v244, v244, v245
	s_nop 0
	ds_write_b128 v228, v[240:243] offset:26112
	ds_write_b32 v229, v244 offset:45056
	s_waitcnt lgkmcnt(0)
	s_barrier
	ds_read_b128 v[162:165], v230 offset:26112
	ds_read_b128 v[166:169], v230 offset:26128
	ds_read_b128 v[170:173], v230 offset:26176
	ds_read_b128 v[174:177], v230 offset:26192
	ds_read_b128 v[178:181], v230 offset:26240
	ds_read_b128 v[182:185], v230 offset:26256
	ds_read_b128 v[186:189], v230 offset:26304
	ds_read_b128 v[190:193], v230 offset:26320
	s_waitcnt lgkmcnt(6)
	v_mfma_scale_f32_32x32x64_f8f6f4 v[2:17], v[34:41], v[162:169], v[2:17], v234, v234 op_sel_hi:[0,0,0]
	s_waitcnt lgkmcnt(4)
	v_mfma_scale_f32_32x32x64_f8f6f4 v[2:17], v[26:33], v[170:177], v[2:17], v234, v234 op_sel_hi:[0,0,0]
	v_min3_f32 v146, v146, v147, v148
	v_min3_f32 v149, v149, v150, v151
	v_min3_f32 v152, v152, v153, v154
	v_min3_f32 v155, v155, v156, v157
	v_min3_f32 v158, v158, v159, v160
	v_min3_f32 v146, v146, v149, v152
	v_min3_f32 v155, v155, v158, v161
	v_min3_f32 v235, v235, v146, v155
	ds_bpermute_b32 v246, v232, v235
	ds_read_b128 v[146:149], v231 offset:34944
	ds_read_b128 v[150:153], v231 offset:34976
	ds_read_b128 v[154:157], v231 offset:35008
	ds_read_b128 v[158:161], v231 offset:35040
	s_waitcnt lgkmcnt(7)
	v_mfma_scale_f32_32x32x64_f8f6f4 v[2:17], v[50:57], v[178:185], v[2:17], v234, v234 op_sel_hi:[0,0,0]
	s_waitcnt lgkmcnt(5)
	v_mfma_scale_f32_32x32x64_f8f6f4 v[2:17], v[42:49], v[186:193], v[2:17], v234, v234 op_sel_hi:[0,0,0]
	s_waitcnt lgkmcnt(0)
	v_min_f32_e32 v246, v235, v246
	ds_write_b32 v233, v246 offset:49152
	v_mfma_scale_f32_32x32x64_f8f6f4 v[146:161], v[18:25], v[162:169], v[146:161], v234, v234 op_sel_hi:[0,0,0]
	v_mfma_scale_f32_32x32x64_f8f6f4 v[146:161], v[130:137], v[170:177], v[146:161], v234, v234 op_sel_hi:[0,0,0]
	v_min3_f32 v2, v2, v3, v4
	v_min3_f32 v5, v5, v6, v7
	v_min3_f32 v8, v8, v9, v10
	v_min3_f32 v11, v11, v12, v13
	v_min3_f32 v14, v14, v15, v16
	v_min3_f32 v2, v2, v5, v8
	v_min3_f32 v11, v11, v14, v17
	v_min_f32_e32 v236, v2, v11
	ds_read_b128 v[2:5], v231 offset:35072
	ds_read_b128 v[6:9], v231 offset:35104
	ds_read_b128 v[10:13], v231 offset:35136
	ds_read_b128 v[14:17], v231 offset:35168
	v_mfma_scale_f32_32x32x64_f8f6f4 v[146:161], v[122:129], v[178:185], v[146:161], v234, v234 op_sel_hi:[0,0,0]
	v_mfma_scale_f32_32x32x64_f8f6f4 v[146:161], v[138:145], v[186:193], v[146:161], v234, v234 op_sel_hi:[0,0,0]
	s_waitcnt lgkmcnt(0)
	v_mfma_scale_f32_32x32x64_f8f6f4 v[2:17], v[98:105], v[162:169], v[2:17], v234, v234 op_sel_hi:[0,0,0]
	v_mfma_scale_f32_32x32x64_f8f6f4 v[2:17], v[90:97], v[170:177], v[2:17], v234, v234 op_sel_hi:[0,0,0]
	v_min3_f32 v146, v146, v147, v148
	v_min3_f32 v149, v149, v150, v151
	v_min3_f32 v152, v152, v153, v154
	v_min3_f32 v155, v155, v156, v157
	v_min3_f32 v158, v158, v159, v160
	v_min3_f32 v146, v146, v149, v152
	v_min3_f32 v155, v155, v158, v161
	v_min3_f32 v236, v236, v146, v155
	ds_read_b128 v[146:149], v231 offset:35200
	ds_read_b128 v[150:153], v231 offset:35232
	ds_read_b128 v[154:157], v231 offset:35264
	ds_read_b128 v[158:161], v231 offset:35296
	v_mfma_scale_f32_32x32x64_f8f6f4 v[2:17], v[114:121], v[178:185], v[2:17], v234, v234 op_sel_hi:[0,0,0]
	v_mfma_scale_f32_32x32x64_f8f6f4 v[2:17], v[106:113], v[186:193], v[2:17], v234, v234 op_sel_hi:[0,0,0]
	s_waitcnt lgkmcnt(0)
	v_mfma_scale_f32_32x32x64_f8f6f4 v[146:161], v[58:65], v[162:169], v[146:161], v234, v234 op_sel_hi:[0,0,0]
	v_mfma_scale_f32_32x32x64_f8f6f4 v[146:161], v[66:73], v[170:177], v[146:161], v234, v234 op_sel_hi:[0,0,0]
	v_min3_f32 v2, v2, v3, v4
	v_min3_f32 v5, v5, v6, v7
	v_min3_f32 v8, v8, v9, v10
	v_min3_f32 v11, v11, v12, v13
	v_min3_f32 v14, v14, v15, v16
	v_min3_f32 v2, v2, v5, v8
	v_min3_f32 v11, v11, v14, v17
	v_min3_f32 v236, v236, v2, v11
	v_mfma_scale_f32_32x32x64_f8f6f4 v[146:161], v[74:81], v[178:185], v[146:161], v234, v234 op_sel_hi:[0,0,0]
	v_mfma_scale_f32_32x32x64_f8f6f4 v[146:161], v[82:89], v[186:193], v[146:161], v234, v234 op_sel_hi:[0,0,0]
	v_cmp_gt_u32_e32 vcc, 0x80, v0
	s_and_saveexec_b64 s[34:35], vcc
	v_lshlrev_b32_e32 v36, 6, v0
	ds_read_b128 v[20:23], v36 offset:38912
	ds_read_b128 v[24:27], v36 offset:38928
	ds_read_b128 v[28:31], v36 offset:38944
	ds_read_b128 v[32:35], v36 offset:38960
	s_mov_b64 exec, s[34:35]
	s_nop 15
	s_nop 3
	v_min3_f32 v146, v146, v147, v148
	v_min3_f32 v149, v149, v150, v151
	v_min3_f32 v152, v152, v153, v154
	v_min3_f32 v155, v155, v156, v157
	v_min3_f32 v158, v158, v159, v160
	v_min3_f32 v146, v146, v149, v152
	v_min3_f32 v155, v155, v158, v161
	v_min3_f32 v236, v236, v146, v155
	ds_bpermute_b32 v246, v232, v236
	s_waitcnt lgkmcnt(0)
	v_min_f32_e32 v246, v236, v246
	ds_write_b32 v233, v246 offset:50176
	s_waitcnt lgkmcnt(0)
	s_barrier
	v_readfirstlane_b32 s2, v1
	s_nop 3
	s_cmp_gt_u32 s2, 1
	s_cbranch_scc1 .Lmain_end
	v_and_b32_e32 v2, 31, v0
	v_lshlrev_b32_e32 v3, 5, v0
	v_and_b32_e32 v3, 0xc00, v3
	v_lshl_or_b32 v8, v2, 2, v3
	v_add_u32_e32 v8, 0xb800, v8
	ds_read2_b32 v[2:3], v8 offset1:32
	ds_read2_b32 v[4:5], v8 offset0:64 offset1:96
	ds_read2_b32 v[6:7], v8 offset0:128 offset1:160
	ds_read2_b32 v[10:11], v8 offset0:192 offset1:224
	s_mov_b32 s8, 0xf800000
	s_lshr_b32 s2, s30, 3
	s_lshl_b32 s2, s2, 7
	s_add_u32 s2, s2, 0x300000
	s_add_u32 s6, s6, s2
	s_addc_u32 s7, s7, 0
	s_mov_b32 s4, 0
	s_mov_b32 s5, 0x41d00000
	s_mov_b32 s16, 0
	s_mov_b32 s17, 0x420e0000
	s_waitcnt lgkmcnt(0)
	v_min3_f32 v2, v2, v3, v4
	v_min3_f32 v5, v5, v6, v7
	v_min3_f32 v2, v2, v10, v11
	v_min_f32_e32 v2, v2, v5
	s_waitcnt lgkmcnt(0)
	v_add_f32_e32 v20, v20, v21
	v_add_f32_e32 v22, v22, v23
	v_add_f32_e32 v24, v24, v25
	v_add_f32_e32 v26, v26, v27
	v_add_f32_e32 v28, v28, v29
	v_add_f32_e32 v30, v30, v31
	v_add_f32_e32 v32, v32, v33
	v_add_f32_e32 v34, v34, v35
	v_add_f32_e32 v20, v20, v22
	v_add_f32_e32 v24, v24, v26
	v_add_f32_e32 v28, v28, v30
	v_add_f32_e32 v32, v32, v34
	v_add_f32_e32 v20, v20, v24
	v_add_f32_e32 v28, v28, v32
	v_add_f32_e32 v20, v20, v28
	v_add_f32_e32 v2, v2, v20
	v_max_f32_e32 v2, 0, v2
	v_mul_f32_e32 v3, 0x4f800000, v2
	v_cmp_gt_f32_e32 vcc, s8, v2
	s_nop 1
	v_cndmask_b32_e32 v2, v2, v3, vcc
	v_sqrt_f32_e32 v3, v2
	s_nop 0
	v_add_u32_e32 v4, -1, v3
	v_fma_f32 v5, -v4, v3, v2
	v_cmp_ge_f32_e64 s[18:19], 0, v5
	v_add_u32_e32 v5, 1, v3
	s_nop 0
	v_cndmask_b32_e64 v4, v3, v4, s[18:19]
	v_fma_f32 v3, -v5, v3, v2
	v_cmp_lt_f32_e64 s[18:19], 0, v3
	s_nop 1
	v_cndmask_b32_e64 v3, v4, v5, s[18:19]
	v_mul_f32_e32 v4, 0x37800000, v3
	v_cndmask_b32_e32 v3, v3, v4, vcc
	v_mov_b32_e32 v4, 0x260
	v_cmp_class_f32_e32 vcc, v2, v4
	s_nop 1
	v_cndmask_b32_e32 v2, v3, v2, vcc
	s_nop 1
	v_add_f32_dpp v3, v2, v2 quad_perm:[1,0,3,2] row_mask:0xf bank_mask:0xf
	s_nop 1
	v_add_f32_dpp v4, v3, v3 quad_perm:[2,3,0,1] row_mask:0xf bank_mask:0xf
	s_nop 1
	v_add_f32_dpp v5, v4, v4 row_half_mirror row_mask:0xf bank_mask:0xf
	s_nop 1
	v_add_f32_dpp v6, v5, v5 row_mirror row_mask:0xf bank_mask:0xf
	s_nop 1
	v_readlane_b32 s12, v6, 0
	v_readlane_b32 s13, v6, 16
	v_readlane_b32 s14, v6, 32
	v_readlane_b32 s15, v6, 48
	s_nop 3
	v_mov_b32_e32 v7, s12
	v_add_f32_e32 v7, s13, v7
	v_mov_b32_e32 v9, s14
	v_add_f32_e32 v9, s15, v9
	v_add_f32_e32 v0, v7, v9
	v_mov_b32_e32 v4, 0
	s_mov_b64 exec, 1
	v_cvt_f64_f32_e32 v[6:7], v0
	v_add_f64 v[8:9], v[6:7], s[4:5]
	global_atomic_add_f64 v[10:11], v4, v[8:9], s[6:7] sc0
	s_waitcnt vmcnt(0)
	v_cmp_le_f64_e32 vcc, s[16:17], v[10:11]
	s_and_saveexec_b64 s[2:3], vcc
	s_cbranch_execz .Lmain_end
	v_add_f64 v[10:11], v[10:11], -s[16:17]
	v_add_f64 v[10:11], v[10:11], v[6:7]
	v_cvt_f32_f64_e32 v0, v[10:11]
	v_mul_f32_e32 v0, 0x38000000, v0
	global_atomic_add_f32 v4, v0, s[10:11]
